# speedup vs baseline: 1.0071x; 1.0071x over previous
.LBB0_35:
	s_getpc_b64 s[88:89]
	v_lshlrev_b32_e32 v20, 6, v206
	v_min_u32_e32 v20, 0x9c0, v20
	v_mov_b32_e32 v21, 0
	s_add_u32 s90, s88, 0x00000200
	s_addc_u32 s91, s89, 0
	v_lshl_add_u64 v[22:23], s[90:91], 0, v[20:21]
	global_load_dword v24, v[22:23], off
	s_andn2_b64 vcc, exec, s[0:1]
	s_cbranch_vccnz .LBB0_45
	s_cmp_gt_u32 s40, 63
	s_cbranch_scc1 .LBB0_45
	v_add3_u32 v0, v206, s69, -1
	s_movk_i32 s0, 0x64
	v_cmp_gt_i32_e32 vcc, s0, v0
	s_and_saveexec_b64 s[0:1], vcc
	s_cbranch_execz .LBB0_45
	v_max_i32_e32 v1, 36, v0
	v_add_u32_e32 v2, s69, v206
	v_sub_u32_e32 v1, v1, v2
	v_add_u32_e32 v1, 64, v1
	v_cmp_lt_u32_e32 vcc, 63, v1
	s_mov_b64 s[4:5], -1
	s_and_saveexec_b64 s[0:1], vcc
	s_cbranch_execz .LBB0_42
	v_lshrrev_b32_e32 v1, 6, v1
	v_add_u32_e32 v6, 1, v1
	v_and_b32_e32 v7, 0x7fffffe, v6
	v_add_u32_e32 v1, 64, v0
	s_mov_b32 s4, s22
	s_mov_b32 s5, s23
	s_mov_b64 s[6:7], 0
	v_mov_b32_e32 v3, 0
	v_mov_b32_e32 v8, v7
	v_mov_b64_e32 v[4:5], v[0:1]
